# merged the two 16-step threshold-score binary searches into one interleaved loop (both DSA copies)
# speedup vs baseline: 1.0068x; 1.0068x over previous
.LBB0_545:
	s_or_b64 exec, exec, s[0:1]
	v_lshl_add_u32 v0, v0, 4, 0
	v_add_u32_e32 v0, 0x23000, v0
	s_waitcnt lgkmcnt(0)
	s_barrier
	ds_read_b32 v0, v0
	v_mov_b32_e32 v3, 0xfc01
	s_mov_b32 s12, 16
	s_waitcnt lgkmcnt(0)
	v_add_u32_e32 v0, 0xffffff80, v0
	v_cvt_f32_i32_e32 v2, v0
	v_mov_b32_e32 v0, 0x3ff
	v_mov_b32_e32 v9, 0xfc01
	v_mov_b32_e32 v8, 0x3ff
.Lthr2_a:
	v_add_u32_e32 v4, v3, v0
	v_add_u32_e32 v10, v9, v8
	v_lshrrev_b32_e32 v5, 1, v4
	v_lshrrev_b32_e32 v11, 1, v10
	v_bfe_u32 v4, v4, 16, 1
	v_bfe_u32 v10, v10, 16, 1
	v_add_u32_e32 v4, -1, v4
	v_add_u32_e32 v10, -1, v10
	v_bitop3_b32 v4, v4, v5, s39 bitop3:0x78
	v_bitop3_b32 v10, v10, v11, s39 bitop3:0x78
	v_cvt_f32_f16_e32 v6, v4
	v_cvt_f32_f16_e32 v12, v10
	v_lshlrev_b32_e32 v4, 16, v4
	v_lshlrev_b32_e32 v10, 16, v10
	v_cmp_lt_u32_e64 s[0:1], v0, v3
	v_cmp_lt_u32_e64 s[28:29], v8, v9
	s_add_i32 s12, s12, -1
	v_sqrt_f32_e64 v6, |v6|
	v_sqrt_f32_e64 v12, |v12|
	v_ceil_f32_e32 v6, v6
	v_ceil_f32_e32 v12, v12
	v_min_f32_e32 v6, 0x42fe0000, v6
	v_min_f32_e32 v12, 0x42fe0000, v12
	v_bfi_b32 v4, s10, v6, v4
	v_bfi_b32 v10, s10, v12, v10
	v_cmp_gt_f32_e32 vcc, v4, v2
	v_cmp_ge_f32_e64 s[30:31], v10, v2
	v_add_u32_e32 v4, 1, v5
	v_add_u32_e32 v10, 1, v11
	v_cndmask_b32_e32 v4, v4, v0, vcc
	v_cndmask_b32_e64 v10, v10, v8, s[30:31]
	s_and_b64 vcc, s[0:1], vcc
	s_and_b64 s[34:35], s[28:29], s[30:31]
	v_cndmask_b32_e32 v3, v3, v5, vcc
	v_cndmask_b32_e64 v9, v9, v11, s[34:35]
	v_cndmask_b32_e64 v0, v0, v4, s[0:1]
	v_cndmask_b32_e64 v8, v8, v10, s[28:29]
	s_cmp_lg_u32 s12, 0
	s_cbranch_scc1 .Lthr2_a
	v_mov_b32_e32 v3, v8
	s_andn2_b64 vcc, exec, s[46:47]
	s_cbranch_vccnz .LBB0_562
	v_readlane_b32 s0, v254, 38
	v_lshlrev_b64 v[4:5], 3, v[42:43]
	v_readlane_b32 s1, v254, 39
	v_bfe_u32 v2, v0, 15, 1
	v_add_u32_e32 v2, -1, v2
	v_lshl_add_u64 v[6:7], s[0:1], 0, v[4:5]
	global_load_dwordx2 v[18:19], v[6:7], off
	global_load_dwordx2 v[16:17], v[6:7], off offset:512
	global_load_dwordx2 v[14:15], v[6:7], off offset:1024
	global_load_dwordx2 v[12:13], v[6:7], off offset:1536
	v_bitop3_b32 v2, v2, v0, s39 bitop3:0x78
	v_cvt_f32_f16_e32 v2, v2
	v_bfe_u32 v6, v3, 15, 1
	v_add_u32_e32 v6, -1, v6
	s_mov_b32 s0, 0xfc01
	v_bitop3_b32 v6, v6, v3, s39 bitop3:0x78
	v_cmp_gt_u32_e32 vcc, s0, v0
	v_mov_b32_e32 v7, 0x7fc00000
	v_cvt_f32_f16_e32 v6, v6
	v_cndmask_b32_e32 v0, v7, v2, vcc
	v_cmp_gt_u32_e32 vcc, s0, v3
	v_ashrrev_i32_e32 v2, 2, v42
	v_readlane_b32 s0, v253, 41
	s_waitcnt vmcnt(8)
	v_and_b32_e32 v21, -4, v2
	v_cndmask_b32_e32 v20, v7, v6, vcc
	v_lshl_add_u32 v2, v42, 8, s0
	v_readlane_b32 s0, v255, 5
	v_readlane_b32 s1, v255, 6
	v_lshl_add_u32 v22, v2, 1, 0
	v_cmp_gt_u32_e32 vcc, 16, v42
	v_lshl_add_u64 v[2:3], s[0:1], 0, v[4:5]
	v_readlane_b32 s0, v254, 11
	s_add_i32 s12, s50, -1
	s_nop 0
	v_add_u32_e32 v23, s0, v21
	s_mov_b32 s0, 0
	s_branch .LBB0_552
